# P9/P10: leading half's re-align barrier moved into the epilogue (its first epilogue VALU overlaps the trailing half's last MFMA segment)
# speedup vs baseline: 1.0035x; 1.0035x over previous
.LBB0_1368:
.LBB0_1370:
	s_ashr_i32 s37, s36, 31
	s_lshl_b64 s[6:7], s[36:37], 14
	v_lshl_or_b32 v22, s34, 7, v186
	s_add_u32 s6, s10, s6
	s_addc_u32 s7, s11, s7
	v_ashrrev_i32_e32 v23, 31, v22
	s_mov_b64 s[6:7], 0x2000
	v_lshl_add_u32 v18, v195, 8, v171
	v_or_b32_e32 v24, 16, v18
	v_or_b32_e32 v26, 32, v18
	v_or_b32_e32 v28, 48, v18
	v_ashrrev_i32_e32 v19, 31, v18
	v_ashrrev_i32_e32 v25, 31, v24
	v_ashrrev_i32_e32 v27, 31, v26
	v_ashrrev_i32_e32 v29, 31, v28
	v_lshlrev_b64 v[18:19], 11, v[18:19]
	v_lshlrev_b64 v[24:25], 11, v[24:25]
	v_lshlrev_b64 v[26:27], 11, v[26:27]
	v_lshlrev_b64 v[28:29], 11, v[28:29]
	v_lshl_add_u64 v[18:19], s[14:15], 0, v[18:19]
	v_lshl_add_u64 v[24:25], s[14:15], 0, v[24:25]
	v_lshl_add_u64 v[26:27], s[14:15], 0, v[26:27]
	v_lshl_add_u64 v[28:29], s[14:15], 0, v[28:29]
	v_lshl_add_u64 v[18:19], v[18:19], 0, v[22:23]
	v_lshl_add_u64 v[24:25], v[24:25], 0, v[22:23]
	v_lshl_add_u64 v[26:27], v[26:27], 0, v[22:23]
	v_lshl_add_u64 v[22:23], v[28:29], 0, v[22:23]
	v_mov_b32_e32 v20, v163
	v_mov_b32_e32 v21, v163
	s_mov_b32 s6, 0x40000
	v_mov_b64_e32 v[6:7], v[234:235]
	v_mov_b64_e32 v[8:9], v[236:237]
	v_mov_b64_e32 v[14:15], v[238:239]
	v_mov_b64_e32 v[16:17], v[240:241]
	v_mov_b64_e32 v[10:11], v[242:243]
	v_mov_b64_e32 v[12:13], v[244:245]
	v_mov_b64_e32 v[2:3], v[246:247]
	v_mov_b64_e32 v[4:5], v[248:249]
	v_pk_fma_f32 v[32:33], v[154:155], s[22:23], v[6:7] op_sel_hi:[1,0,1]
	v_pk_fma_f32 v[28:29], v[158:159], s[22:23], v[14:15] op_sel_hi:[1,0,1]
	v_pk_fma_f32 v[154:155], v[156:157], s[22:23], v[8:9] op_sel_hi:[1,0,1]
	v_min_f32_e32 v28, 0x40e00000, v28
	v_min_f32_e32 v29, 0x40e00000, v29
	v_min_f32_e32 v32, 0x40e00000, v32
	v_min_f32_e32 v33, 0x40e00000, v33
	v_pk_mul_f32 v[156:157], v[28:29], s[24:25] op_sel_hi:[1,0]
	v_pk_fma_f32 v[30:31], v[160:161], s[22:23], v[16:17] op_sel_hi:[1,0,1]
	v_pk_mul_f32 v[160:161], v[32:33], s[24:25] op_sel_hi:[1,0]
	v_exp_f32_e32 v156, v156
	v_exp_f32_e32 v157, v157
	v_exp_f32_e32 v160, v160
	v_exp_f32_e32 v161, v161
	v_min_f32_e32 v30, 0x40e00000, v30
	v_min_f32_e32 v31, 0x40e00000, v31
	v_min_f32_e32 v154, 0x40e00000, v154
	v_min_f32_e32 v155, 0x40e00000, v155
	v_pk_mul_f32 v[158:159], v[30:31], s[24:25] op_sel_hi:[1,0]
	v_pk_mul_f32 v[168:169], v[154:155], s[24:25] op_sel_hi:[1,0]
	v_exp_f32_e32 v158, v158
	v_exp_f32_e32 v159, v159
	v_pk_add_f32 v[156:157], v[156:157], 1.0 op_sel_hi:[1,0]
	v_exp_f32_e32 v168, v168
	v_exp_f32_e32 v169, v169
	v_pk_add_f32 v[160:161], v[160:161], 1.0 op_sel_hi:[1,0]
	v_rcp_f32_e32 v156, v156
	v_rcp_f32_e32 v157, v157
	v_rcp_f32_e32 v160, v160
	v_rcp_f32_e32 v161, v161
	v_pk_fma_f32 v[150:151], v[150:151], s[22:23], v[10:11] op_sel_hi:[1,0,1]
	v_pk_fma_f32 v[146:147], v[146:147], s[22:23], v[2:3] op_sel_hi:[1,0,1]
	v_med3_f32 v150, v150, s87, v189
	v_med3_f32 v151, v151, s87, v189
	v_pk_add_f32 v[158:159], v[158:159], 1.0 op_sel_hi:[1,0]
	v_med3_f32 v146, v146, s87, v189
	v_med3_f32 v147, v147, s87, v189
	v_pk_add_f32 v[150:151], v[150:151], 1.0 op_sel_hi:[1,0]
	v_pk_add_f32 v[168:169], v[168:169], 1.0 op_sel_hi:[1,0]
	v_rcp_f32_e32 v158, v158
	v_rcp_f32_e32 v159, v159
	v_pk_mul_f32 v[28:29], v[28:29], v[156:157]
	v_pk_add_f32 v[146:147], v[146:147], 1.0 op_sel_hi:[1,0]
	v_rcp_f32_e32 v168, v168
	v_rcp_f32_e32 v169, v169
	v_pk_mul_f32 v[32:33], v[32:33], v[160:161]
	v_pk_mul_f32 v[28:29], v[150:151], v[28:29]
	v_pk_fma_f32 v[152:153], v[152:153], s[22:23], v[12:13] op_sel_hi:[1,0,1]
	v_pk_mul_f32 v[32:33], v[146:147], v[32:33]
	v_cvt_pk_fp8_f32 v20, v28, v29
	v_pk_fma_f32 v[148:149], v[148:149], s[22:23], v[4:5] op_sel_hi:[1,0,1]
	v_med3_f32 v152, v152, s87, v189
	v_med3_f32 v153, v153, s87, v189
	v_cvt_pk_fp8_f32 v21, v32, v33
	v_med3_f32 v148, v148, s87, v189
	v_med3_f32 v149, v149, s87, v189
	v_pk_add_f32 v[152:153], v[152:153], 1.0 op_sel_hi:[1,0]
	v_pk_mul_f32 v[30:31], v[30:31], v[158:159]
	v_pk_fma_f32 v[142:143], v[142:143], s[22:23], v[14:15] op_sel_hi:[1,0,1]
	v_pk_add_f32 v[148:149], v[148:149], 1.0 op_sel_hi:[1,0]
	v_pk_mul_f32 v[154:155], v[154:155], v[168:169]
	v_pk_mul_f32 v[28:29], v[152:153], v[30:31]
	v_pk_mul_f32 v[30:31], v[148:149], v[154:155]
	v_cvt_pk_fp8_f32 v20, v28, v29 op_sel:[0,0,1]
	v_min_f32_e32 v28, 0x40e00000, v142
	v_min_f32_e32 v29, 0x40e00000, v143
	v_cvt_pk_fp8_f32 v21, v30, v31 op_sel:[0,0,1]
	v_pk_mul_f32 v[30:31], v[28:29], s[24:25] op_sel_hi:[1,0]
	v_pk_fma_f32 v[32:33], v[138:139], s[22:23], v[10:11] op_sel_hi:[1,0,1]
	v_exp_f32_e32 v30, v30
	s_and_b64 vcc, exec, s[18:19]
	s_cbranch_vccz .Lp9_lbar
	s_barrier
.Lp9_lbar:
	v_exp_f32_e32 v31, v31
	v_pk_fma_f32 v[138:139], v[144:145], s[22:23], v[16:17] op_sel_hi:[1,0,1]
	v_med3_f32 v32, v32, s87, v189
	v_min_f32_e32 v138, 0x40e00000, v138
	v_pk_add_f32 v[30:31], v[30:31], 1.0 op_sel_hi:[1,0]
	v_min_f32_e32 v139, 0x40e00000, v139
	v_rcp_f32_e32 v30, v30
	v_rcp_f32_e32 v31, v31
	v_pk_mul_f32 v[142:143], v[138:139], s[24:25] op_sel_hi:[1,0]
	v_med3_f32 v33, v33, s87, v189
	v_exp_f32_e32 v142, v142
	v_exp_f32_e32 v143, v143
	v_pk_mul_f32 v[28:29], v[28:29], v[30:31]
	v_pk_add_f32 v[30:31], v[32:33], 1.0 op_sel_hi:[1,0]
	v_pk_fma_f32 v[32:33], v[140:141], s[22:23], v[12:13] op_sel_hi:[1,0,1]
	v_pk_mul_f32 v[30:31], v[30:31], v[28:29]
	v_pk_add_f32 v[28:29], v[142:143], 1.0 op_sel_hi:[1,0]
	v_med3_f32 v32, v32, s87, v189
	v_rcp_f32_e32 v28, v28
	v_rcp_f32_e32 v29, v29
	v_med3_f32 v33, v33, s87, v189
	v_pk_add_f32 v[32:33], v[32:33], 1.0 op_sel_hi:[1,0]
	v_pk_fma_f32 v[136:137], v[136:137], s[22:23], v[8:9] op_sel_hi:[1,0,1]
	v_pk_mul_f32 v[28:29], v[138:139], v[28:29]
	v_min_f32_e32 v136, 0x40e00000, v136
	v_pk_mul_f32 v[32:33], v[32:33], v[28:29]
	v_pk_fma_f32 v[28:29], v[134:135], s[22:23], v[6:7] op_sel_hi:[1,0,1]
	v_min_f32_e32 v137, 0x40e00000, v137
	v_min_f32_e32 v28, 0x40e00000, v28
	v_min_f32_e32 v29, 0x40e00000, v29
	v_pk_mul_f32 v[134:135], v[28:29], s[24:25] op_sel_hi:[1,0]
	v_pk_mul_f32 v[138:139], v[136:137], s[24:25] op_sel_hi:[1,0]
	v_exp_f32_e32 v134, v134
	v_exp_f32_e32 v135, v135
	v_exp_f32_e32 v138, v138
	v_exp_f32_e32 v139, v139
	v_pk_fma_f32 v[130:131], v[130:131], s[22:23], v[2:3] op_sel_hi:[1,0,1]
	v_pk_add_f32 v[134:135], v[134:135], 1.0 op_sel_hi:[1,0]
	v_med3_f32 v130, v130, s87, v189
	v_rcp_f32_e32 v134, v134
	v_rcp_f32_e32 v135, v135
	v_med3_f32 v131, v131, s87, v189
	v_pk_add_f32 v[130:131], v[130:131], 1.0 op_sel_hi:[1,0]
	v_pk_fma_f32 v[132:133], v[132:133], s[22:23], v[4:5] op_sel_hi:[1,0,1]
	v_pk_mul_f32 v[28:29], v[28:29], v[134:135]
	v_med3_f32 v132, v132, s87, v189
	v_pk_mul_f32 v[130:131], v[130:131], v[28:29]
	v_pk_add_f32 v[28:29], v[138:139], 1.0 op_sel_hi:[1,0]
	v_med3_f32 v133, v133, s87, v189
	v_rcp_f32_e32 v28, v28
	v_rcp_f32_e32 v29, v29
	v_pk_fma_f32 v[122:123], v[122:123], s[22:23], v[10:11] op_sel_hi:[1,0,1]
	v_pk_fma_f32 v[118:119], v[118:119], s[22:23], v[6:7] op_sel_hi:[1,0,1]
	v_med3_f32 v122, v122, s87, v189
	v_pk_mul_f32 v[134:135], v[136:137], v[28:29]
	v_mov_b32_e32 v29, v163
	v_cvt_pk_fp8_f32 v29, v130, v131
	v_mov_b32_e32 v28, v163
	v_cvt_pk_fp8_f32 v28, v30, v31
	v_pk_add_f32 v[30:31], v[132:133], 1.0 op_sel_hi:[1,0]
	v_med3_f32 v123, v123, s87, v189
	v_pk_mul_f32 v[30:31], v[30:31], v[134:135]
	v_cvt_pk_fp8_f32 v28, v32, v33 op_sel:[0,0,1]
	v_cvt_pk_fp8_f32 v29, v30, v31 op_sel:[0,0,1]
	v_pk_fma_f32 v[30:31], v[126:127], s[22:23], v[14:15] op_sel_hi:[1,0,1]
	v_pk_fma_f32 v[126:127], v[128:129], s[22:23], v[16:17] op_sel_hi:[1,0,1]
	v_min_f32_e32 v30, 0x40e00000, v30
	v_min_f32_e32 v31, 0x40e00000, v31
	v_pk_mul_f32 v[32:33], v[30:31], s[24:25] op_sel_hi:[1,0]
	v_min_f32_e32 v126, 0x40e00000, v126
	v_exp_f32_e32 v32, v32
	v_exp_f32_e32 v33, v33
	v_min_f32_e32 v127, 0x40e00000, v127
	v_pk_mul_f32 v[128:129], v[126:127], s[24:25] op_sel_hi:[1,0]
	v_min_f32_e32 v118, 0x40e00000, v118
	v_pk_add_f32 v[32:33], v[32:33], 1.0 op_sel_hi:[1,0]
	v_exp_f32_e32 v128, v128
	v_rcp_f32_e32 v32, v32
	v_rcp_f32_e32 v33, v33
	v_exp_f32_e32 v129, v129
	v_min_f32_e32 v119, 0x40e00000, v119
	v_pk_fma_f32 v[120:121], v[120:121], s[22:23], v[8:9] op_sel_hi:[1,0,1]
	v_pk_mul_f32 v[30:31], v[30:31], v[32:33]
	v_pk_add_f32 v[32:33], v[122:123], 1.0 op_sel_hi:[1,0]
	v_pk_fma_f32 v[122:123], v[124:125], s[22:23], v[12:13] op_sel_hi:[1,0,1]
	v_pk_mul_f32 v[30:31], v[32:33], v[30:31]
	v_pk_add_f32 v[32:33], v[128:129], 1.0 op_sel_hi:[1,0]
	v_med3_f32 v122, v122, s87, v189
	v_rcp_f32_e32 v32, v32
	v_rcp_f32_e32 v33, v33
	v_med3_f32 v123, v123, s87, v189
	v_pk_add_f32 v[122:123], v[122:123], 1.0 op_sel_hi:[1,0]
	v_min_f32_e32 v120, 0x40e00000, v120
	v_pk_mul_f32 v[32:33], v[126:127], v[32:33]
	v_min_f32_e32 v121, 0x40e00000, v121
	v_pk_mul_f32 v[32:33], v[122:123], v[32:33]
	v_pk_mul_f32 v[122:123], v[118:119], s[24:25] op_sel_hi:[1,0]
	v_pk_mul_f32 v[124:125], v[120:121], s[24:25] op_sel_hi:[1,0]
	v_exp_f32_e32 v122, v122
	v_exp_f32_e32 v123, v123
	v_exp_f32_e32 v124, v124
	v_exp_f32_e32 v125, v125
	v_pk_fma_f32 v[114:115], v[114:115], s[22:23], v[2:3] op_sel_hi:[1,0,1]
	v_pk_add_f32 v[122:123], v[122:123], 1.0 op_sel_hi:[1,0]
	v_med3_f32 v114, v114, s87, v189
	v_rcp_f32_e32 v122, v122
	v_rcp_f32_e32 v123, v123
	v_med3_f32 v115, v115, s87, v189
	v_pk_add_f32 v[114:115], v[114:115], 1.0 op_sel_hi:[1,0]
	v_pk_fma_f32 v[116:117], v[116:117], s[22:23], v[4:5] op_sel_hi:[1,0,1]
	v_pk_mul_f32 v[118:119], v[118:119], v[122:123]
	v_med3_f32 v116, v116, s87, v189
	v_pk_mul_f32 v[114:115], v[114:115], v[118:119]
	v_pk_add_f32 v[118:119], v[124:125], 1.0 op_sel_hi:[1,0]
	v_med3_f32 v117, v117, s87, v189
	v_rcp_f32_e32 v118, v118
	v_rcp_f32_e32 v119, v119
	v_pk_fma_f32 v[106:107], v[106:107], s[22:23], v[10:11] op_sel_hi:[1,0,1]
	v_pk_fma_f32 v[102:103], v[102:103], s[22:23], v[6:7] op_sel_hi:[1,0,1]
	v_med3_f32 v106, v106, s87, v189
	v_pk_mul_f32 v[118:119], v[120:121], v[118:119]
	v_mov_b32_e32 v121, v163
	v_cvt_pk_fp8_f32 v121, v114, v115
	v_mov_b32_e32 v120, v163
	v_cvt_pk_fp8_f32 v120, v30, v31
	v_pk_add_f32 v[30:31], v[116:117], 1.0 op_sel_hi:[1,0]
	v_med3_f32 v107, v107, s87, v189
	v_pk_mul_f32 v[30:31], v[30:31], v[118:119]
	v_cvt_pk_fp8_f32 v120, v32, v33 op_sel:[0,0,1]
	v_cvt_pk_fp8_f32 v121, v30, v31 op_sel:[0,0,1]
	v_pk_fma_f32 v[30:31], v[110:111], s[22:23], v[14:15] op_sel_hi:[1,0,1]
	v_pk_fma_f32 v[110:111], v[112:113], s[22:23], v[16:17] op_sel_hi:[1,0,1]
	v_min_f32_e32 v30, 0x40e00000, v30
	v_min_f32_e32 v31, 0x40e00000, v31
	v_pk_mul_f32 v[32:33], v[30:31], s[24:25] op_sel_hi:[1,0]
	v_min_f32_e32 v110, 0x40e00000, v110
	v_exp_f32_e32 v32, v32
	v_exp_f32_e32 v33, v33
	v_min_f32_e32 v111, 0x40e00000, v111
	v_pk_mul_f32 v[112:113], v[110:111], s[24:25] op_sel_hi:[1,0]
	v_min_f32_e32 v102, 0x40e00000, v102
	v_pk_add_f32 v[32:33], v[32:33], 1.0 op_sel_hi:[1,0]
	v_exp_f32_e32 v112, v112
	v_rcp_f32_e32 v32, v32
	v_rcp_f32_e32 v33, v33
	v_exp_f32_e32 v113, v113
	v_min_f32_e32 v103, 0x40e00000, v103
	v_pk_fma_f32 v[104:105], v[104:105], s[22:23], v[8:9] op_sel_hi:[1,0,1]
	v_pk_mul_f32 v[30:31], v[30:31], v[32:33]
	v_pk_add_f32 v[32:33], v[106:107], 1.0 op_sel_hi:[1,0]
	v_pk_fma_f32 v[106:107], v[108:109], s[22:23], v[12:13] op_sel_hi:[1,0,1]
	v_pk_mul_f32 v[30:31], v[32:33], v[30:31]
	v_pk_add_f32 v[32:33], v[112:113], 1.0 op_sel_hi:[1,0]
	v_med3_f32 v106, v106, s87, v189
	v_rcp_f32_e32 v32, v32
	v_rcp_f32_e32 v33, v33
	v_med3_f32 v107, v107, s87, v189
	v_pk_add_f32 v[106:107], v[106:107], 1.0 op_sel_hi:[1,0]
	v_min_f32_e32 v104, 0x40e00000, v104
	v_pk_mul_f32 v[32:33], v[110:111], v[32:33]
	v_min_f32_e32 v105, 0x40e00000, v105
	v_pk_mul_f32 v[32:33], v[106:107], v[32:33]
	v_pk_mul_f32 v[106:107], v[102:103], s[24:25] op_sel_hi:[1,0]
	v_pk_mul_f32 v[108:109], v[104:105], s[24:25] op_sel_hi:[1,0]
	v_exp_f32_e32 v106, v106
	v_exp_f32_e32 v107, v107
	v_exp_f32_e32 v108, v108
	v_exp_f32_e32 v109, v109
	v_pk_fma_f32 v[98:99], v[98:99], s[22:23], v[2:3] op_sel_hi:[1,0,1]
	v_pk_add_f32 v[106:107], v[106:107], 1.0 op_sel_hi:[1,0]
	v_med3_f32 v98, v98, s87, v189
	v_rcp_f32_e32 v106, v106
	v_rcp_f32_e32 v107, v107
	v_med3_f32 v99, v99, s87, v189
	v_pk_add_f32 v[98:99], v[98:99], 1.0 op_sel_hi:[1,0]
	v_pk_fma_f32 v[100:101], v[100:101], s[22:23], v[4:5] op_sel_hi:[1,0,1]
	v_pk_mul_f32 v[102:103], v[102:103], v[106:107]
	v_med3_f32 v100, v100, s87, v189
	v_pk_mul_f32 v[98:99], v[98:99], v[102:103]
	v_pk_add_f32 v[102:103], v[108:109], 1.0 op_sel_hi:[1,0]
	v_med3_f32 v101, v101, s87, v189
	v_rcp_f32_e32 v102, v102
	v_rcp_f32_e32 v103, v103
	s_nop 0
	v_pk_mul_f32 v[102:103], v[104:105], v[102:103]
	v_mov_b32_e32 v104, v163
	v_mov_b32_e32 v105, v163
	v_cvt_pk_fp8_f32 v104, v30, v31
	v_cvt_pk_fp8_f32 v105, v98, v99
	v_pk_add_f32 v[30:31], v[100:101], 1.0 op_sel_hi:[1,0]
	v_cvt_pk_fp8_f32 v104, v32, v33 op_sel:[0,0,1]
	v_pk_mul_f32 v[30:31], v[30:31], v[102:103]
	s_nop 0
	v_cvt_pk_fp8_f32 v105, v30, v31 op_sel:[0,0,1]
	global_store_dwordx2 v[18:19], v[20:21], off
	global_store_dwordx2 v[24:25], v[28:29], off
	global_store_dwordx2 v[26:27], v[120:121], off
	global_store_dwordx2 v[22:23], v[104:105], off
	v_pk_fma_f32 v[20:21], v[94:95], s[22:23], v[14:15] op_sel_hi:[1,0,1]
	v_pk_fma_f32 v[26:27], v[96:97], s[22:23], v[16:17] op_sel_hi:[1,0,1]
	v_min_f32_e32 v20, 0x40e00000, v20
	v_min_f32_e32 v21, 0x40e00000, v21
	v_pk_mul_f32 v[22:23], v[20:21], s[24:25] op_sel_hi:[1,0]
	v_min_f32_e32 v26, 0x40e00000, v26
	v_exp_f32_e32 v22, v22
	v_exp_f32_e32 v23, v23
	v_min_f32_e32 v27, 0x40e00000, v27
	v_pk_mul_f32 v[28:29], v[26:27], s[24:25] op_sel_hi:[1,0]
	v_pk_fma_f32 v[24:25], v[90:91], s[22:23], v[10:11] op_sel_hi:[1,0,1]
	v_pk_add_f32 v[22:23], v[22:23], 1.0 op_sel_hi:[1,0]
	v_exp_f32_e32 v28, v28
	v_rcp_f32_e32 v22, v22
	v_rcp_f32_e32 v23, v23
	v_exp_f32_e32 v29, v29
	v_med3_f32 v24, v24, s87, v189
	v_med3_f32 v25, v25, s87, v189
	v_pk_mul_f32 v[20:21], v[20:21], v[22:23]
	v_pk_add_f32 v[22:23], v[24:25], 1.0 op_sel_hi:[1,0]
	v_pk_fma_f32 v[24:25], v[92:93], s[22:23], v[12:13] op_sel_hi:[1,0,1]
	v_pk_mul_f32 v[20:21], v[22:23], v[20:21]
	v_pk_add_f32 v[22:23], v[28:29], 1.0 op_sel_hi:[1,0]
	v_med3_f32 v24, v24, s87, v189
	v_rcp_f32_e32 v22, v22
	v_rcp_f32_e32 v23, v23
	v_med3_f32 v25, v25, s87, v189
	v_pk_add_f32 v[24:25], v[24:25], 1.0 op_sel_hi:[1,0]
	v_pk_fma_f32 v[30:31], v[88:89], s[22:23], v[8:9] op_sel_hi:[1,0,1]
	v_pk_mul_f32 v[22:23], v[26:27], v[22:23]
	v_min_f32_e32 v30, 0x40e00000, v30
	v_pk_mul_f32 v[22:23], v[24:25], v[22:23]
	v_pk_fma_f32 v[24:25], v[86:87], s[22:23], v[6:7] op_sel_hi:[1,0,1]
	v_min_f32_e32 v31, 0x40e00000, v31
	v_min_f32_e32 v24, 0x40e00000, v24
	v_min_f32_e32 v25, 0x40e00000, v25
	v_pk_mul_f32 v[26:27], v[24:25], s[24:25] op_sel_hi:[1,0]
	v_pk_mul_f32 v[32:33], v[30:31], s[24:25] op_sel_hi:[1,0]
	v_exp_f32_e32 v26, v26
	v_exp_f32_e32 v27, v27
	v_exp_f32_e32 v32, v32
	v_exp_f32_e32 v33, v33
	v_pk_fma_f32 v[28:29], v[82:83], s[22:23], v[2:3] op_sel_hi:[1,0,1]
	v_pk_add_f32 v[26:27], v[26:27], 1.0 op_sel_hi:[1,0]
	v_med3_f32 v28, v28, s87, v189
	v_rcp_f32_e32 v26, v26
	v_rcp_f32_e32 v27, v27
	v_med3_f32 v29, v29, s87, v189
	v_pk_mul_f32 v[24:25], v[24:25], v[26:27]
	v_pk_add_f32 v[26:27], v[28:29], 1.0 op_sel_hi:[1,0]
	v_pk_fma_f32 v[28:29], v[84:85], s[22:23], v[4:5] op_sel_hi:[1,0,1]
	v_pk_mul_f32 v[24:25], v[26:27], v[24:25]
	v_pk_add_f32 v[26:27], v[32:33], 1.0 op_sel_hi:[1,0]
	v_med3_f32 v28, v28, s87, v189
	v_rcp_f32_e32 v26, v26
	v_rcp_f32_e32 v27, v27
	v_med3_f32 v29, v29, s87, v189
	v_pk_mul_f32 v[26:27], v[30:31], v[26:27]
	v_mov_b32_e32 v30, v163
	v_mov_b32_e32 v31, v163
	v_cvt_pk_fp8_f32 v30, v20, v21
	v_cvt_pk_fp8_f32 v31, v24, v25
	v_pk_add_f32 v[20:21], v[28:29], 1.0 op_sel_hi:[1,0]
	v_pk_fma_f32 v[24:25], v[74:75], s[22:23], v[10:11] op_sel_hi:[1,0,1]
	v_pk_mul_f32 v[20:21], v[20:21], v[26:27]
	v_cvt_pk_fp8_f32 v30, v22, v23 op_sel:[0,0,1]
	v_cvt_pk_fp8_f32 v31, v20, v21 op_sel:[0,0,1]
	v_add_co_u32_e32 v20, vcc, s6, v18
	v_pk_fma_f32 v[26:27], v[80:81], s[22:23], v[16:17] op_sel_hi:[1,0,1]
	s_nop 0
	v_addc_co_u32_e32 v21, vcc, 0, v19, vcc
	global_store_dwordx2 v[20:21], v[30:31], off
	v_pk_fma_f32 v[20:21], v[78:79], s[22:23], v[14:15] op_sel_hi:[1,0,1]
	v_min_f32_e32 v26, 0x40e00000, v26
	v_min_f32_e32 v20, 0x40e00000, v20
	v_min_f32_e32 v21, 0x40e00000, v21
	v_pk_mul_f32 v[22:23], v[20:21], s[24:25] op_sel_hi:[1,0]
	v_min_f32_e32 v27, 0x40e00000, v27
	v_exp_f32_e32 v22, v22
	v_exp_f32_e32 v23, v23
	v_pk_mul_f32 v[28:29], v[26:27], s[24:25] op_sel_hi:[1,0]
	v_med3_f32 v24, v24, s87, v189
	v_exp_f32_e32 v28, v28
	v_pk_add_f32 v[22:23], v[22:23], 1.0 op_sel_hi:[1,0]
	v_exp_f32_e32 v29, v29
	v_rcp_f32_e32 v22, v22
	v_rcp_f32_e32 v23, v23
	v_med3_f32 v25, v25, s87, v189
	v_pk_fma_f32 v[30:31], v[72:73], s[22:23], v[8:9] op_sel_hi:[1,0,1]
	s_mov_b32 s6, 0x48000
	v_pk_mul_f32 v[20:21], v[20:21], v[22:23]
	v_pk_add_f32 v[22:23], v[24:25], 1.0 op_sel_hi:[1,0]
	v_pk_fma_f32 v[24:25], v[76:77], s[22:23], v[12:13] op_sel_hi:[1,0,1]
	v_pk_mul_f32 v[20:21], v[22:23], v[20:21]
	v_pk_add_f32 v[22:23], v[28:29], 1.0 op_sel_hi:[1,0]
	v_med3_f32 v24, v24, s87, v189
	v_rcp_f32_e32 v22, v22
	v_rcp_f32_e32 v23, v23
	v_med3_f32 v25, v25, s87, v189
	v_pk_add_f32 v[24:25], v[24:25], 1.0 op_sel_hi:[1,0]
	v_min_f32_e32 v30, 0x40e00000, v30
	v_pk_mul_f32 v[22:23], v[26:27], v[22:23]
	v_min_f32_e32 v31, 0x40e00000, v31
	v_pk_mul_f32 v[22:23], v[24:25], v[22:23]
	v_pk_fma_f32 v[24:25], v[70:71], s[22:23], v[6:7] op_sel_hi:[1,0,1]
	v_pk_mul_f32 v[32:33], v[30:31], s[24:25] op_sel_hi:[1,0]
	v_min_f32_e32 v24, 0x40e00000, v24
	v_min_f32_e32 v25, 0x40e00000, v25
	v_pk_mul_f32 v[26:27], v[24:25], s[24:25] op_sel_hi:[1,0]
	v_exp_f32_e32 v32, v32
	v_exp_f32_e32 v26, v26
	v_exp_f32_e32 v27, v27
	v_exp_f32_e32 v33, v33
	v_pk_fma_f32 v[28:29], v[66:67], s[22:23], v[2:3] op_sel_hi:[1,0,1]
	v_pk_add_f32 v[26:27], v[26:27], 1.0 op_sel_hi:[1,0]
	s_nop 0
	v_rcp_f32_e32 v26, v26
	v_rcp_f32_e32 v27, v27
	v_med3_f32 v28, v28, s87, v189
	v_med3_f32 v29, v29, s87, v189
	v_pk_mul_f32 v[24:25], v[24:25], v[26:27]
	v_pk_add_f32 v[26:27], v[28:29], 1.0 op_sel_hi:[1,0]
	v_pk_fma_f32 v[28:29], v[68:69], s[22:23], v[4:5] op_sel_hi:[1,0,1]
	v_pk_mul_f32 v[24:25], v[26:27], v[24:25]
	v_pk_add_f32 v[26:27], v[32:33], 1.0 op_sel_hi:[1,0]
	v_med3_f32 v28, v28, s87, v189
	v_rcp_f32_e32 v26, v26
	v_rcp_f32_e32 v27, v27
	v_med3_f32 v29, v29, s87, v189
	v_pk_mul_f32 v[26:27], v[30:31], v[26:27]
	v_mov_b32_e32 v30, v163
	v_mov_b32_e32 v31, v163
	v_cvt_pk_fp8_f32 v30, v20, v21
	v_cvt_pk_fp8_f32 v31, v24, v25
	v_pk_add_f32 v[20:21], v[28:29], 1.0 op_sel_hi:[1,0]
	v_pk_fma_f32 v[24:25], v[58:59], s[22:23], v[10:11] op_sel_hi:[1,0,1]
	v_pk_mul_f32 v[20:21], v[20:21], v[26:27]
	v_cvt_pk_fp8_f32 v30, v22, v23 op_sel:[0,0,1]
	v_cvt_pk_fp8_f32 v31, v20, v21 op_sel:[0,0,1]
	v_add_co_u32_e32 v20, vcc, s6, v18
	v_pk_fma_f32 v[26:27], v[64:65], s[22:23], v[16:17] op_sel_hi:[1,0,1]
	s_nop 0
	v_addc_co_u32_e32 v21, vcc, 0, v19, vcc
	global_store_dwordx2 v[20:21], v[30:31], off
	v_pk_fma_f32 v[20:21], v[62:63], s[22:23], v[14:15] op_sel_hi:[1,0,1]
	v_min_f32_e32 v26, 0x40e00000, v26
	v_min_f32_e32 v20, 0x40e00000, v20
	v_min_f32_e32 v21, 0x40e00000, v21
	v_pk_mul_f32 v[22:23], v[20:21], s[24:25] op_sel_hi:[1,0]
	v_min_f32_e32 v27, 0x40e00000, v27
	v_exp_f32_e32 v22, v22
	v_exp_f32_e32 v23, v23
	v_pk_mul_f32 v[28:29], v[26:27], s[24:25] op_sel_hi:[1,0]
	v_med3_f32 v24, v24, s87, v189
	v_exp_f32_e32 v28, v28
	v_pk_add_f32 v[22:23], v[22:23], 1.0 op_sel_hi:[1,0]
	v_exp_f32_e32 v29, v29
	v_rcp_f32_e32 v22, v22
	v_rcp_f32_e32 v23, v23
	v_med3_f32 v25, v25, s87, v189
	v_pk_fma_f32 v[30:31], v[56:57], s[22:23], v[8:9] op_sel_hi:[1,0,1]
	s_mov_b32 s6, 0x50000
	v_pk_mul_f32 v[20:21], v[20:21], v[22:23]
	v_pk_add_f32 v[22:23], v[24:25], 1.0 op_sel_hi:[1,0]
	v_pk_fma_f32 v[24:25], v[60:61], s[22:23], v[12:13] op_sel_hi:[1,0,1]
	v_pk_mul_f32 v[20:21], v[22:23], v[20:21]
	v_pk_add_f32 v[22:23], v[28:29], 1.0 op_sel_hi:[1,0]
	v_med3_f32 v24, v24, s87, v189
	v_rcp_f32_e32 v22, v22
	v_rcp_f32_e32 v23, v23
	v_med3_f32 v25, v25, s87, v189
	v_pk_add_f32 v[24:25], v[24:25], 1.0 op_sel_hi:[1,0]
	v_min_f32_e32 v30, 0x40e00000, v30
	v_pk_mul_f32 v[22:23], v[26:27], v[22:23]
	v_min_f32_e32 v31, 0x40e00000, v31
	v_pk_mul_f32 v[22:23], v[24:25], v[22:23]
	v_pk_fma_f32 v[24:25], v[54:55], s[22:23], v[6:7] op_sel_hi:[1,0,1]
	v_pk_mul_f32 v[32:33], v[30:31], s[24:25] op_sel_hi:[1,0]
	v_min_f32_e32 v24, 0x40e00000, v24
	v_min_f32_e32 v25, 0x40e00000, v25
	v_pk_mul_f32 v[26:27], v[24:25], s[24:25] op_sel_hi:[1,0]
	v_exp_f32_e32 v32, v32
	v_exp_f32_e32 v26, v26
	v_exp_f32_e32 v27, v27
	v_exp_f32_e32 v33, v33
	v_pk_fma_f32 v[28:29], v[50:51], s[22:23], v[2:3] op_sel_hi:[1,0,1]
	v_pk_fma_f32 v[14:15], v[46:47], s[22:23], v[14:15] op_sel_hi:[1,0,1]
	v_pk_add_f32 v[26:27], v[26:27], 1.0 op_sel_hi:[1,0]
	v_med3_f32 v28, v28, s87, v189
	v_rcp_f32_e32 v26, v26
	v_rcp_f32_e32 v27, v27
	v_med3_f32 v29, v29, s87, v189
	v_min_f32_e32 v14, 0x40e00000, v14
	v_min_f32_e32 v15, 0x40e00000, v15
	v_pk_mul_f32 v[24:25], v[24:25], v[26:27]
	v_pk_add_f32 v[26:27], v[28:29], 1.0 op_sel_hi:[1,0]
	v_pk_fma_f32 v[28:29], v[52:53], s[22:23], v[4:5] op_sel_hi:[1,0,1]
	v_pk_mul_f32 v[24:25], v[26:27], v[24:25]
	v_pk_add_f32 v[26:27], v[32:33], 1.0 op_sel_hi:[1,0]
	v_med3_f32 v28, v28, s87, v189
	v_rcp_f32_e32 v26, v26
	v_rcp_f32_e32 v27, v27
	v_med3_f32 v29, v29, s87, v189
	v_pk_fma_f32 v[16:17], v[48:49], s[22:23], v[16:17] op_sel_hi:[1,0,1]
	v_pk_fma_f32 v[10:11], v[42:43], s[22:23], v[10:11] op_sel_hi:[1,0,1]
	v_pk_mul_f32 v[26:27], v[30:31], v[26:27]
	v_mov_b32_e32 v30, v163
	v_mov_b32_e32 v31, v163
	v_cvt_pk_fp8_f32 v30, v20, v21
	v_cvt_pk_fp8_f32 v31, v24, v25
	v_pk_add_f32 v[20:21], v[28:29], 1.0 op_sel_hi:[1,0]
	v_min_f32_e32 v16, 0x40e00000, v16
	v_pk_mul_f32 v[20:21], v[20:21], v[26:27]
	v_cvt_pk_fp8_f32 v30, v22, v23 op_sel:[0,0,1]
	v_cvt_pk_fp8_f32 v31, v20, v21 op_sel:[0,0,1]
	v_add_co_u32_e32 v20, vcc, s6, v18
	v_min_f32_e32 v17, 0x40e00000, v17
	s_nop 0
	v_addc_co_u32_e32 v21, vcc, 0, v19, vcc
	global_store_dwordx2 v[20:21], v[30:31], off
	v_pk_mul_f32 v[20:21], v[14:15], s[24:25] op_sel_hi:[1,0]
	v_pk_mul_f32 v[22:23], v[16:17], s[24:25] op_sel_hi:[1,0]
	v_exp_f32_e32 v20, v20
	v_exp_f32_e32 v21, v21
	v_exp_f32_e32 v22, v22
	v_exp_f32_e32 v23, v23
	v_med3_f32 v10, v10, s87, v189
	v_pk_add_f32 v[20:21], v[20:21], 1.0 op_sel_hi:[1,0]
	v_med3_f32 v11, v11, s87, v189
	v_rcp_f32_e32 v20, v20
	v_rcp_f32_e32 v21, v21
	v_pk_add_f32 v[10:11], v[10:11], 1.0 op_sel_hi:[1,0]
	v_pk_fma_f32 v[12:13], v[44:45], s[22:23], v[12:13] op_sel_hi:[1,0,1]
	v_pk_fma_f32 v[6:7], v[38:39], s[22:23], v[6:7] op_sel_hi:[1,0,1]
	v_pk_mul_f32 v[14:15], v[14:15], v[20:21]
	v_med3_f32 v12, v12, s87, v189
	v_pk_mul_f32 v[10:11], v[10:11], v[14:15]
	v_pk_add_f32 v[14:15], v[22:23], 1.0 op_sel_hi:[1,0]
	v_med3_f32 v13, v13, s87, v189
	v_rcp_f32_e32 v14, v14
	v_rcp_f32_e32 v15, v15
	v_pk_add_f32 v[12:13], v[12:13], 1.0 op_sel_hi:[1,0]
	v_min_f32_e32 v6, 0x40e00000, v6
	v_min_f32_e32 v7, 0x40e00000, v7
	v_pk_mul_f32 v[14:15], v[16:17], v[14:15]
	v_pk_fma_f32 v[8:9], v[40:41], s[22:23], v[8:9] op_sel_hi:[1,0,1]
	v_pk_mul_f32 v[12:13], v[12:13], v[14:15]
	v_pk_mul_f32 v[14:15], v[6:7], s[24:25] op_sel_hi:[1,0]
	v_min_f32_e32 v8, 0x40e00000, v8
	v_exp_f32_e32 v14, v14
	v_exp_f32_e32 v15, v15
	v_min_f32_e32 v9, 0x40e00000, v9
	v_pk_mul_f32 v[16:17], v[8:9], s[24:25] op_sel_hi:[1,0]
	v_pk_fma_f32 v[2:3], v[34:35], s[22:23], v[2:3] op_sel_hi:[1,0,1]
	v_pk_add_f32 v[14:15], v[14:15], 1.0 op_sel_hi:[1,0]
	v_exp_f32_e32 v16, v16
	v_rcp_f32_e32 v14, v14
	v_rcp_f32_e32 v15, v15
	v_exp_f32_e32 v17, v17
	v_med3_f32 v2, v2, s87, v189
	v_med3_f32 v3, v3, s87, v189
	v_pk_mul_f32 v[6:7], v[6:7], v[14:15]
	v_pk_add_f32 v[2:3], v[2:3], 1.0 op_sel_hi:[1,0]
	v_pk_fma_f32 v[4:5], v[36:37], s[22:23], v[4:5] op_sel_hi:[1,0,1]
	v_pk_mul_f32 v[2:3], v[2:3], v[6:7]
	v_pk_add_f32 v[6:7], v[16:17], 1.0 op_sel_hi:[1,0]
	v_med3_f32 v4, v4, s87, v189
	v_rcp_f32_e32 v6, v6
	v_rcp_f32_e32 v7, v7
	v_med3_f32 v5, v5, s87, v189
	v_pk_mul_f32 v[6:7], v[8:9], v[6:7]
	v_mov_b32_e32 v8, v163
	v_mov_b32_e32 v9, v163
	v_cvt_pk_fp8_f32 v8, v10, v11
	v_cvt_pk_fp8_f32 v9, v2, v3
	v_pk_add_f32 v[2:3], v[4:5], 1.0 op_sel_hi:[1,0]
	v_cvt_pk_fp8_f32 v8, v12, v13 op_sel:[0,0,1]
	v_pk_mul_f32 v[2:3], v[2:3], v[6:7]
	s_nop 0
	v_cvt_pk_fp8_f32 v9, v2, v3 op_sel:[0,0,1]
	v_add_co_u32_e32 v2, vcc, 0x58000, v18
	s_nop 1
	v_addc_co_u32_e32 v3, vcc, 0, v19, vcc
	s_andn2_b64 vcc, exec, s[4:5]
	s_mov_b64 s[4:5], -1
	global_store_dwordx2 v[2:3], v[8:9], off
	s_cbranch_vccnz .LBB0_1348
	s_andn2_b64 vcc, exec, s[12:13]
	s_cbranch_vccnz .LBB0_1347
	s_barrier
	s_branch .LBB0_1347

.LBB0_1443:
	s_mov_b32 s100, s85
	s_mov_b32 s101, 0
	s_lshl_b64 s[100:101], s[100:101], 19
	s_add_u32 s100, s100, s18
	s_addc_u32 s101, s101, s19
	s_lshl_b32 vcc_lo, s10, 8
	s_add_u32 s100, s100, vcc_lo
	s_addc_u32 s101, s101, 0
	s_ashr_i32 s41, s40, 31
	s_lshl_b64 s[40:41], s[40:41], 13
	v_lshl_or_b32 v20, s10, 8, v183
	s_add_u32 s40, s12, s40
	s_addc_u32 s41, s13, s41
	v_ashrrev_i32_e32 v21, 31, v20
	v_lshl_add_u64 v[2:3], v[20:21], 2, s[40:41]
	global_load_dwordx4 v[14:17], v[2:3], off
	global_load_dwordx4 v[10:13], v[2:3], off offset:16
	global_load_dwordx4 v[6:9], v[2:3], off offset:128
	s_nop 0
	global_load_dwordx4 v[2:5], v[2:3], off offset:144
	v_mov_b32_e32 v24, 0
	v_mov_b32_e32 v25, 0
	v_mov_b32_e32 v26, 0
	v_mov_b32_e32 v27, 0
	v_mov_b32_e32 v28, 0
	v_mov_b32_e32 v29, 0
	v_mov_b32_e32 v30, 0
	v_mov_b32_e32 v31, 0
	v_lshl_add_u32 v18, s85, 8, v1
	v_mov_b32_e32 v174, 0
	v_mov_b32_e32 v175, 0
	v_ashrrev_i32_e32 v19, 31, v18
	v_or_b32_e32 v22, 16, v18
	v_or_b32_e32 v176, 32, v18
	v_or_b32_e32 v178, 48, v18
	v_lshlrev_b64 v[18:19], 11, v[18:19]
	v_ashrrev_i32_e32 v23, 31, v22
	v_lshl_add_u64 v[18:19], s[18:19], 0, v[18:19]
	v_lshlrev_b64 v[22:23], 11, v[22:23]
	v_lshl_add_u64 v[18:19], v[18:19], 0, v[20:21]
	v_lshl_add_u64 v[22:23], s[18:19], 0, v[22:23]
	v_lshl_add_u64 v[180:181], v[22:23], 0, v[20:21]
	v_mov_b32_e32 v32, 0
	v_mov_b32_e32 v33, 0
	v_ashrrev_i32_e32 v177, 31, v176
	v_ashrrev_i32_e32 v179, 31, v178
	v_lshlrev_b64 v[176:177], 11, v[176:177]
	v_lshlrev_b64 v[178:179], 11, v[178:179]
	v_lshl_add_u64 v[176:177], s[18:19], 0, v[176:177]
	v_lshl_add_u64 v[178:179], s[18:19], 0, v[178:179]
	v_lshl_add_u64 v[176:177], v[176:177], 0, v[20:21]
	v_lshl_add_u64 v[178:179], v[178:179], 0, v[20:21]
	v_lshl_add_u64 v[188:189], v[18:19], 0, s[14:15]
	v_lshl_add_u64 v[190:191], v[18:19], 0, s[24:25]
	v_lshl_add_u64 v[22:23], v[18:19], 0, s[26:27]
	v_lshl_add_u64 v[20:21], v[18:19], 0, s[28:29]
	s_and_b64 vcc, exec, s[22:23]
	s_cbranch_vccz .Lp10_lbar
	s_barrier
.Lp10_lbar:
	s_waitcnt vmcnt(0)
	v_pk_fma_f32 v[158:159], v[158:159], s[30:31], v[14:15] op_sel_hi:[1,0,1]
	v_pk_fma_f32 v[154:155], v[154:155], s[30:31], v[10:11] op_sel_hi:[1,0,1]
	v_pk_fma_f32 v[138:139], v[138:139], s[30:31], v[6:7] op_sel_hi:[1,0,1]
	v_pk_fma_f32 v[130:131], v[130:131], s[30:31], v[2:3] op_sel_hi:[1,0,1]
	v_cvt_pk_fp8_f32 v24, v158, v159
	v_cvt_pk_fp8_f32 v25, v154, v155
	v_pk_fma_f32 v[150:151], v[150:151], s[30:31], v[14:15] op_sel_hi:[1,0,1]
	v_pk_fma_f32 v[146:147], v[146:147], s[30:31], v[10:11] op_sel_hi:[1,0,1]
	v_cvt_pk_fp8_f32 v26, v138, v139
	v_cvt_pk_fp8_f32 v27, v130, v131
	v_pk_fma_f32 v[126:127], v[126:127], s[30:31], v[6:7] op_sel_hi:[1,0,1]
	v_pk_fma_f32 v[122:123], v[122:123], s[30:31], v[2:3] op_sel_hi:[1,0,1]
	v_cvt_pk_fp8_f32 v28, v150, v151
	v_cvt_pk_fp8_f32 v29, v146, v147
	v_pk_fma_f32 v[160:161], v[160:161], s[30:31], v[16:17] op_sel_hi:[1,0,1]
	v_pk_fma_f32 v[156:157], v[156:157], s[30:31], v[12:13] op_sel_hi:[1,0,1]
	v_cvt_pk_fp8_f32 v30, v126, v127
	v_cvt_pk_fp8_f32 v31, v122, v123
	v_pk_fma_f32 v[140:141], v[140:141], s[30:31], v[8:9] op_sel_hi:[1,0,1]
	v_pk_fma_f32 v[132:133], v[132:133], s[30:31], v[4:5] op_sel_hi:[1,0,1]
	v_pk_fma_f32 v[114:115], v[114:115], s[30:31], v[6:7] op_sel_hi:[1,0,1]
	v_pk_fma_f32 v[106:107], v[106:107], s[30:31], v[2:3] op_sel_hi:[1,0,1]
	v_cvt_pk_fp8_f32 v24, v160, v161 op_sel:[0,0,1]
	v_cvt_pk_fp8_f32 v25, v156, v157 op_sel:[0,0,1]
	v_pk_fma_f32 v[152:153], v[152:153], s[30:31], v[16:17] op_sel_hi:[1,0,1]
	v_pk_fma_f32 v[148:149], v[148:149], s[30:31], v[12:13] op_sel_hi:[1,0,1]
	v_cvt_pk_fp8_f32 v174, v114, v115
	v_cvt_pk_fp8_f32 v26, v140, v141 op_sel:[0,0,1]
	v_cvt_pk_fp8_f32 v27, v132, v133 op_sel:[0,0,1]
	v_cvt_pk_fp8_f32 v175, v106, v107
	v_pk_fma_f32 v[128:129], v[128:129], s[30:31], v[8:9] op_sel_hi:[1,0,1]
	v_pk_fma_f32 v[124:125], v[124:125], s[30:31], v[4:5] op_sel_hi:[1,0,1]
	v_cvt_pk_fp8_f32 v28, v152, v153 op_sel:[0,0,1]
	v_cvt_pk_fp8_f32 v29, v148, v149 op_sel:[0,0,1]
	v_cvt_pk_fp8_f32 v30, v128, v129 op_sel:[0,0,1]
	v_cvt_pk_fp8_f32 v31, v124, v125 op_sel:[0,0,1]
	v_mov_b32_e32 v222, v24
	v_mov_b32_e32 v223, v25
	v_mov_b32_e32 v224, v26
	v_mov_b32_e32 v225, v27
	s_nop 1
	v_permlane16_swap_b32 v222, v224
	v_permlane16_swap_b32 v223, v225
	v_mov_b32_e32 v226, v28
	v_mov_b32_e32 v227, v29
	v_mov_b32_e32 v228, v30
	v_mov_b32_e32 v229, v31
	s_nop 1
	v_permlane16_swap_b32 v226, v228
	v_permlane16_swap_b32 v227, v229
	v_pk_fma_f32 v[24:25], v[116:117], s[30:31], v[8:9] op_sel_hi:[1,0,1]
	v_pk_fma_f32 v[26:27], v[108:109], s[30:31], v[4:5] op_sel_hi:[1,0,1]
	v_cvt_pk_fp8_f32 v174, v24, v25 op_sel:[0,0,1]
	v_cvt_pk_fp8_f32 v175, v26, v27 op_sel:[0,0,1]
	v_pk_fma_f32 v[24:25], v[118:119], s[30:31], v[14:15] op_sel_hi:[1,0,1]
	v_pk_fma_f32 v[26:27], v[110:111], s[30:31], v[10:11] op_sel_hi:[1,0,1]
	v_mov_b32_e32 v28, 0
	v_mov_b32_e32 v29, 0
	v_cvt_pk_fp8_f32 v28, v24, v25
	v_cvt_pk_fp8_f32 v29, v26, v27
	v_pk_fma_f32 v[142:143], v[142:143], s[30:31], v[14:15] op_sel_hi:[1,0,1]
	v_pk_fma_f32 v[134:135], v[134:135], s[30:31], v[10:11] op_sel_hi:[1,0,1]
	v_cvt_pk_fp8_f32 v32, v142, v143
	v_cvt_pk_fp8_f32 v33, v134, v135
	v_pk_fma_f32 v[24:25], v[120:121], s[30:31], v[16:17] op_sel_hi:[1,0,1]
	v_pk_fma_f32 v[26:27], v[112:113], s[30:31], v[12:13] op_sel_hi:[1,0,1]
	v_cvt_pk_fp8_f32 v28, v24, v25 op_sel:[0,0,1]
	v_cvt_pk_fp8_f32 v29, v26, v27 op_sel:[0,0,1]
	v_pk_fma_f32 v[24:25], v[102:103], s[30:31], v[6:7] op_sel_hi:[1,0,1]
	v_pk_fma_f32 v[26:27], v[98:99], s[30:31], v[2:3] op_sel_hi:[1,0,1]
	v_mov_b32_e32 v30, 0
	v_mov_b32_e32 v31, 0
	v_pk_fma_f32 v[144:145], v[144:145], s[30:31], v[16:17] op_sel_hi:[1,0,1]
	v_pk_fma_f32 v[136:137], v[136:137], s[30:31], v[12:13] op_sel_hi:[1,0,1]
	v_cvt_pk_fp8_f32 v30, v24, v25
	v_cvt_pk_fp8_f32 v31, v26, v27
	v_cvt_pk_fp8_f32 v32, v144, v145 op_sel:[0,0,1]
	v_cvt_pk_fp8_f32 v33, v136, v137 op_sel:[0,0,1]
	v_pk_fma_f32 v[24:25], v[104:105], s[30:31], v[8:9] op_sel_hi:[1,0,1]
	v_pk_fma_f32 v[26:27], v[100:101], s[30:31], v[4:5] op_sel_hi:[1,0,1]
	v_cvt_pk_fp8_f32 v30, v24, v25 op_sel:[0,0,1]
	v_cvt_pk_fp8_f32 v31, v26, v27 op_sel:[0,0,1]
	v_mov_b32_e32 v230, v32
	v_mov_b32_e32 v231, v33
	v_mov_b32_e32 v232, v174
	v_mov_b32_e32 v233, v175
	s_nop 1
	v_permlane16_swap_b32 v230, v232
	v_permlane16_swap_b32 v231, v233
	v_mov_b32_e32 v234, v28
	v_mov_b32_e32 v235, v29
	v_mov_b32_e32 v236, v30
	v_mov_b32_e32 v237, v31
	s_nop 1
	v_permlane16_swap_b32 v234, v236
	v_permlane16_swap_b32 v235, v237
	v_pk_fma_f32 v[24:25], v[94:95], s[30:31], v[14:15] op_sel_hi:[1,0,1]
	v_pk_fma_f32 v[26:27], v[90:91], s[30:31], v[10:11] op_sel_hi:[1,0,1]
	v_mov_b32_e32 v28, 0
	v_mov_b32_e32 v29, 0
	v_cvt_pk_fp8_f32 v28, v24, v25
	v_cvt_pk_fp8_f32 v29, v26, v27
	v_pk_fma_f32 v[24:25], v[96:97], s[30:31], v[16:17] op_sel_hi:[1,0,1]
	v_pk_fma_f32 v[26:27], v[92:93], s[30:31], v[12:13] op_sel_hi:[1,0,1]
	v_cvt_pk_fp8_f32 v28, v24, v25 op_sel:[0,0,1]
	v_cvt_pk_fp8_f32 v29, v26, v27 op_sel:[0,0,1]
	v_pk_fma_f32 v[24:25], v[82:83], s[30:31], v[6:7] op_sel_hi:[1,0,1]
	v_pk_fma_f32 v[26:27], v[70:71], s[30:31], v[2:3] op_sel_hi:[1,0,1]
	v_mov_b32_e32 v30, 0
	v_mov_b32_e32 v31, 0
	v_cvt_pk_fp8_f32 v30, v24, v25
	v_cvt_pk_fp8_f32 v31, v26, v27
	v_pk_fma_f32 v[24:25], v[84:85], s[30:31], v[8:9] op_sel_hi:[1,0,1]
	v_pk_fma_f32 v[26:27], v[72:73], s[30:31], v[4:5] op_sel_hi:[1,0,1]
	v_cvt_pk_fp8_f32 v30, v24, v25 op_sel:[0,0,1]
	v_cvt_pk_fp8_f32 v31, v26, v27 op_sel:[0,0,1]
	v_add_co_u32_e32 v24, vcc, s58, v18
	v_pk_fma_f32 v[26:27], v[66:67], s[30:31], v[10:11] op_sel_hi:[1,0,1]
	s_nop 0
	v_addc_co_u32_e32 v25, vcc, 0, v19, vcc
	v_mov_b32_e32 v238, v28
	v_mov_b32_e32 v239, v29
	v_mov_b32_e32 v240, v30
	v_mov_b32_e32 v241, v31
	s_nop 1
	v_permlane16_swap_b32 v238, v240
	v_permlane16_swap_b32 v239, v241
	v_pk_fma_f32 v[24:25], v[78:79], s[30:31], v[14:15] op_sel_hi:[1,0,1]
	v_mov_b32_e32 v28, 0
	v_mov_b32_e32 v29, 0
	v_cvt_pk_fp8_f32 v28, v24, v25
	v_cvt_pk_fp8_f32 v29, v26, v27
	v_pk_fma_f32 v[24:25], v[80:81], s[30:31], v[16:17] op_sel_hi:[1,0,1]
	v_pk_fma_f32 v[26:27], v[68:69], s[30:31], v[12:13] op_sel_hi:[1,0,1]
	v_cvt_pk_fp8_f32 v28, v24, v25 op_sel:[0,0,1]
	v_cvt_pk_fp8_f32 v29, v26, v27 op_sel:[0,0,1]
	v_pk_fma_f32 v[24:25], v[54:55], s[30:31], v[6:7] op_sel_hi:[1,0,1]
	v_pk_fma_f32 v[26:27], v[42:43], s[30:31], v[2:3] op_sel_hi:[1,0,1]
	v_mov_b32_e32 v30, 0
	v_mov_b32_e32 v31, 0
	v_cvt_pk_fp8_f32 v30, v24, v25
	v_cvt_pk_fp8_f32 v31, v26, v27
	v_pk_fma_f32 v[24:25], v[56:57], s[30:31], v[8:9] op_sel_hi:[1,0,1]
	v_pk_fma_f32 v[26:27], v[44:45], s[30:31], v[4:5] op_sel_hi:[1,0,1]
	v_cvt_pk_fp8_f32 v30, v24, v25 op_sel:[0,0,1]
	v_cvt_pk_fp8_f32 v31, v26, v27 op_sel:[0,0,1]
	v_add_co_u32_e32 v24, vcc, s82, v18
	v_pk_fma_f32 v[26:27], v[46:47], s[30:31], v[10:11] op_sel_hi:[1,0,1]
	s_nop 0
	v_addc_co_u32_e32 v25, vcc, 0, v19, vcc
	v_mov_b32_e32 v242, v28
	v_mov_b32_e32 v243, v29
	v_mov_b32_e32 v244, v30
	v_mov_b32_e32 v245, v31
	s_nop 1
	v_permlane16_swap_b32 v242, v244
	v_permlane16_swap_b32 v243, v245
	v_pk_fma_f32 v[24:25], v[50:51], s[30:31], v[14:15] op_sel_hi:[1,0,1]
	v_mov_b32_e32 v28, 0
	v_mov_b32_e32 v29, 0
	v_cvt_pk_fp8_f32 v28, v24, v25
	v_cvt_pk_fp8_f32 v29, v26, v27
	v_pk_fma_f32 v[24:25], v[52:53], s[30:31], v[16:17] op_sel_hi:[1,0,1]
	v_pk_fma_f32 v[26:27], v[48:49], s[30:31], v[12:13] op_sel_hi:[1,0,1]
	v_cvt_pk_fp8_f32 v28, v24, v25 op_sel:[0,0,1]
	v_cvt_pk_fp8_f32 v29, v26, v27 op_sel:[0,0,1]
	v_pk_fma_f32 v[24:25], v[74:75], s[30:31], v[6:7] op_sel_hi:[1,0,1]
	v_pk_fma_f32 v[26:27], v[86:87], s[30:31], v[2:3] op_sel_hi:[1,0,1]
	v_mov_b32_e32 v30, 0
	v_mov_b32_e32 v31, 0
	v_cvt_pk_fp8_f32 v30, v24, v25
	v_cvt_pk_fp8_f32 v31, v26, v27
	v_pk_fma_f32 v[24:25], v[76:77], s[30:31], v[8:9] op_sel_hi:[1,0,1]
	v_pk_fma_f32 v[26:27], v[88:89], s[30:31], v[4:5] op_sel_hi:[1,0,1]
	v_cvt_pk_fp8_f32 v30, v24, v25 op_sel:[0,0,1]
	v_cvt_pk_fp8_f32 v31, v26, v27 op_sel:[0,0,1]
	v_add_co_u32_e32 v24, vcc, s83, v18
	v_pk_fma_f32 v[14:15], v[38:39], s[30:31], v[14:15] op_sel_hi:[1,0,1]
	s_nop 0
	v_addc_co_u32_e32 v25, vcc, 0, v19, vcc
	v_mov_b32_e32 v246, v28
	v_mov_b32_e32 v247, v29
	v_mov_b32_e32 v248, v30
	v_mov_b32_e32 v249, v31
	s_nop 1
	v_permlane16_swap_b32 v246, v248
	v_permlane16_swap_b32 v247, v249
	v_mov_b32_e32 v22, 0
	v_cvt_pk_fp8_f32 v22, v14, v15
	v_pk_fma_f32 v[10:11], v[34:35], s[30:31], v[10:11] op_sel_hi:[1,0,1]
	v_mov_b32_e32 v23, 0
	v_cvt_pk_fp8_f32 v23, v10, v11
	v_pk_fma_f32 v[10:11], v[40:41], s[30:31], v[16:17] op_sel_hi:[1,0,1]
	v_pk_fma_f32 v[6:7], v[58:59], s[30:31], v[6:7] op_sel_hi:[1,0,1]
	v_cvt_pk_fp8_f32 v22, v10, v11 op_sel:[0,0,1]
	v_pk_fma_f32 v[2:3], v[62:63], s[30:31], v[2:3] op_sel_hi:[1,0,1]
	v_mov_b32_e32 v10, 0
	v_mov_b32_e32 v11, 0
	v_cvt_pk_fp8_f32 v10, v6, v7
	v_cvt_pk_fp8_f32 v11, v2, v3
	v_pk_fma_f32 v[12:13], v[36:37], s[30:31], v[12:13] op_sel_hi:[1,0,1]
	v_pk_fma_f32 v[2:3], v[60:61], s[30:31], v[8:9] op_sel_hi:[1,0,1]
	v_cvt_pk_fp8_f32 v23, v12, v13 op_sel:[0,0,1]
	v_pk_fma_f32 v[4:5], v[64:65], s[30:31], v[4:5] op_sel_hi:[1,0,1]
	v_cvt_pk_fp8_f32 v10, v2, v3 op_sel:[0,0,1]
	v_cvt_pk_fp8_f32 v11, v4, v5 op_sel:[0,0,1]
	v_add_co_u32_e32 v2, vcc, s84, v18
	s_nop 1
	v_addc_co_u32_e32 v3, vcc, 0, v19, vcc
	s_andn2_b64 vcc, exec, s[6:7]
	s_mov_b64 s[6:7], -1
	v_mov_b32_e32 v250, v22
	v_mov_b32_e32 v251, v23
	v_mov_b32_e32 v252, v10
	v_mov_b32_e32 v253, v11
	s_nop 1
	v_permlane16_swap_b32 v250, v252
	v_permlane16_swap_b32 v251, v253
	s_cbranch_vccnz .LBB0_1434
	s_andn2_b64 vcc, exec, s[16:17]
	s_cbranch_vccnz .LBB0_1433
	s_barrier
	s_branch .LBB0_1433
